# baseline (speedup 1.0000x reference)
.LBB1_79:
	s_andn2_b64 vcc, exec, s[6:7]
	s_cbranch_vccnz .LBB1_81
	s_waitcnt vmcnt(0)
.LBB1_81:
	s_barrier
	s_setprio 2
	s_mov_b32 m0, s37
	v_add_u32_e32 v0, s48, v211
	global_load_lds_dwordx4 v0, s[10:11]
	v_add_u32_e32 v0, s48, v212
	s_mov_b32 m0, s38
	s_nop 0
	global_load_lds_dwordx4 v0, s[10:11]
	s_setprio 0
	s_setprio 2
	v_mbcnt_lo_u32_b32 v248, -1, 0
	v_mbcnt_hi_u32_b32 v248, -1, v248
	v_mul_u32_u24_e32 v251, 57, v248
	v_lshrrev_b32_e32 v251, 9, v251
	v_mul_u32_u24_e32 v252, 9, v251
	v_sub_u32_e32 v252, v248, v252
	v_mul_u32_u24_e32 v253, 11, v252
	v_lshrrev_b32_e32 v253, 5, v253
	v_mul_u32_u24_e32 v254, 3, v253
	v_sub_u32_e32 v254, v252, v254
	v_add_u32_e32 v253, -1, v253
	v_mul_lo_u32 v253, v253, s50
	v_add3_u32 v253, v253, v254, -1
	v_lshlrev_b32_e32 v253, 9, v253
	v_lshl_add_u32 v253, v251, 7, v253
	v_add_u32_e32 v248, s47, v253
	v_add_u32_e32 v249, 0x10000, v206
	v_add_u32_e32 v250, 0x10000, v213
	v_readlane_b32 s3, v248, 1
	s_mov_b32 m0, s39
	s_nop 1
	v_add_u32_e32 v0, s3, v206
	global_load_lds_dwordx4 v0, s[18:19]
	v_add_u32_e32 v0, s3, v213
	s_mov_b32 m0, s40
	s_nop 0
	global_load_lds_dwordx4 v0, s[18:19]
	s_setprio 0
	s_setprio 2
	s_mov_b32 m0, s41
	v_add_u32_e32 v0, s48, v214
	global_load_lds_dwordx4 v0, s[10:11]
	v_add_u32_e32 v0, s48, v215
	s_mov_b32 m0, s42
	s_nop 0
	global_load_lds_dwordx4 v0, s[10:11]
	s_setprio 0
	s_add_i32 s3, s47, 0xfe00
	s_lshl_b32 s6, s50, 23
	v_add_u32_e32 v128, s48, v218
	s_mov_b32 s8, 0
	s_movk_i32 s7, 0x180
	s_barrier
.Lk_first:
	ds_read_b128 v[130:133], v219 offset:32768
	ds_read_b128 v[134:137], v219 offset:33792
	ds_read_b128 v[138:141], v219 offset:34816
	ds_read_b128 v[142:145], v219 offset:35840
	ds_read_b128 v[178:181], v219 offset:49152
	ds_read_b128 v[182:185], v219 offset:50176
	ds_read_b128 v[186:189], v219 offset:51200
	ds_read_b128 v[190:193], v219 offset:52224
	ds_read_b128 v[146:149], v220
	ds_read_b128 v[150:153], v220 offset:1024
	ds_read_b128 v[154:157], v221
	ds_read_b128 v[158:161], v221 offset:1024
	ds_read_b128 v[162:165], v222
	ds_read_b128 v[166:169], v222 offset:1024
	ds_read_b128 v[170:173], v223
	ds_read_b128 v[174:177], v223 offset:1024
	s_add_i32 s12, s8, 1
	v_readlane_b32 s9, v248, s12
	s_mov_b32 m0, s43
	s_nop 1
	v_add_u32_e32 v251, s9, v249
	global_load_lds_dwordx4 v251, s[18:19]
	v_add_u32_e32 v251, s9, v250
	s_mov_b32 m0, s44
	s_nop 0
	global_load_lds_dwordx4 v251, s[18:19]
	s_waitcnt lgkmcnt(0)
	s_barrier
	s_setprio 1
	v_mfma_f32_16x16x32_f16 v[124:127], v[130:133], v[146:149], 0
	v_mfma_f32_16x16x32_f16 v[120:123], v[138:141], v[146:149], 0
	v_mfma_f32_16x16x32_f16 v[116:119], v[130:133], v[154:157], 0
	v_mfma_f32_16x16x32_f16 v[112:115], v[138:141], v[154:157], 0
	v_mfma_f32_16x16x32_f16 v[108:111], v[130:133], v[162:165], 0
	v_mfma_f32_16x16x32_f16 v[104:107], v[138:141], v[162:165], 0
	v_mfma_f32_16x16x32_f16 v[100:103], v[130:133], v[170:173], 0
	v_mfma_f32_16x16x32_f16 v[96:99], v[138:141], v[170:173], 0
	v_mfma_f32_16x16x32_f16 v[124:127], v[134:137], v[150:153], v[124:127]
	v_mfma_f32_16x16x32_f16 v[120:123], v[142:145], v[150:153], v[120:123]
	v_mfma_f32_16x16x32_f16 v[116:119], v[134:137], v[158:161], v[116:119]
	v_mfma_f32_16x16x32_f16 v[112:115], v[142:145], v[158:161], v[112:115]
	v_mfma_f32_16x16x32_f16 v[108:111], v[134:137], v[166:169], v[108:111]
	v_mfma_f32_16x16x32_f16 v[104:107], v[142:145], v[166:169], v[104:107]
	v_mfma_f32_16x16x32_f16 v[100:103], v[134:137], v[174:177], v[100:103]
	v_mfma_f32_16x16x32_f16 v[96:99], v[142:145], v[174:177], v[96:99]
	v_mfma_f32_16x16x32_f16 v[52:55], v[178:181], v[146:149], 0
	v_mfma_f32_16x16x32_f16 v[40:43], v[186:189], v[146:149], 0
	v_mfma_f32_16x16x32_f16 v[36:39], v[178:181], v[154:157], 0
	v_mfma_f32_16x16x32_f16 v[32:35], v[186:189], v[154:157], 0
	v_mfma_f32_16x16x32_f16 v[28:31], v[178:181], v[162:165], 0
	v_mfma_f32_16x16x32_f16 v[24:27], v[186:189], v[162:165], 0
	v_mfma_f32_16x16x32_f16 v[20:23], v[178:181], v[170:173], 0
	v_mfma_f32_16x16x32_f16 v[16:19], v[186:189], v[170:173], 0
	v_mfma_f32_16x16x32_f16 v[52:55], v[182:185], v[150:153], v[52:55]
	v_mfma_f32_16x16x32_f16 v[40:43], v[190:193], v[150:153], v[40:43]
	v_mfma_f32_16x16x32_f16 v[36:39], v[182:185], v[158:161], v[36:39]
	v_mfma_f32_16x16x32_f16 v[32:35], v[190:193], v[158:161], v[32:35]
	v_mfma_f32_16x16x32_f16 v[28:31], v[182:185], v[166:169], v[28:31]
	v_mfma_f32_16x16x32_f16 v[24:27], v[190:193], v[166:169], v[24:27]
	v_mfma_f32_16x16x32_f16 v[20:23], v[182:185], v[174:177], v[20:23]
	v_mfma_f32_16x16x32_f16 v[16:19], v[190:193], v[174:177], v[16:19]
	s_setprio 0
	s_barrier
	ds_read_b128 v[146:149], v220 offset:16384
	ds_read_b128 v[150:153], v220 offset:17408
	ds_read_b128 v[154:157], v221 offset:16384
	ds_read_b128 v[158:161], v221 offset:17408
	ds_read_b128 v[162:165], v222 offset:16384
	ds_read_b128 v[166:169], v222 offset:17408
	ds_read_b128 v[170:173], v223 offset:16384
	ds_read_b128 v[174:177], v223 offset:17408
	v_add_u32_e32 v129, s7, v128
	s_mov_b32 m0, s22
	v_add_u32_e32 v194, 0xffffff80, v129
	global_load_lds_dwordx4 v194, s[10:11]
	v_add_u32_e32 v194, 0x47f80, v129
	s_mov_b32 m0, s23
	s_add_i32 s9, s8, 2
	global_load_lds_dwordx4 v194, s[10:11]
	v_readlane_b32 s13, v248, s9
	s_mov_b32 m0, s21
	s_nop 1
	v_add_u32_e32 v194, s13, v206
	global_load_lds_dwordx4 v194, s[18:19]
	v_add_u32_e32 v194, s13, v213
	s_mov_b32 m0, s24
	s_nop 0
	global_load_lds_dwordx4 v194, s[18:19]
	s_mov_b32 m0, s25
	v_add_u32_e32 v194, 0x8ff80, v129
	global_load_lds_dwordx4 v194, s[10:11]
	v_add_u32_e32 v194, 0xd7f80, v129
	s_mov_b32 m0, s26
	s_nop 0
	global_load_lds_dwordx4 v194, s[10:11]
	s_waitcnt vmcnt(8) lgkmcnt(0)
	s_barrier
	s_setprio 1
	v_mfma_f32_16x16x32_f16 v[12:15], v[130:133], v[146:149], 0
	v_mfma_f32_16x16x32_f16 v[8:11], v[138:141], v[146:149], 0
	v_mfma_f32_16x16x32_f16 v[4:7], v[130:133], v[154:157], 0
	v_mfma_f32_16x16x32_f16 v[0:3], v[138:141], v[154:157], 0
	v_mfma_f32_16x16x32_f16 v[44:47], v[130:133], v[162:165], 0
	v_mfma_f32_16x16x32_f16 v[48:51], v[138:141], v[162:165], 0
	v_mfma_f32_16x16x32_f16 v[56:59], v[130:133], v[170:173], 0
	v_mfma_f32_16x16x32_f16 v[60:63], v[138:141], v[170:173], 0
	v_mfma_f32_16x16x32_f16 v[12:15], v[134:137], v[150:153], v[12:15]
	v_mfma_f32_16x16x32_f16 v[8:11], v[142:145], v[150:153], v[8:11]
	v_mfma_f32_16x16x32_f16 v[4:7], v[134:137], v[158:161], v[4:7]
	v_mfma_f32_16x16x32_f16 v[0:3], v[142:145], v[158:161], v[0:3]
	v_mfma_f32_16x16x32_f16 v[44:47], v[134:137], v[166:169], v[44:47]
	v_mfma_f32_16x16x32_f16 v[48:51], v[142:145], v[166:169], v[48:51]
	v_mfma_f32_16x16x32_f16 v[56:59], v[134:137], v[174:177], v[56:59]
	v_mfma_f32_16x16x32_f16 v[60:63], v[142:145], v[174:177], v[60:63]
	v_mfma_f32_16x16x32_f16 v[64:67], v[178:181], v[146:149], 0
	v_mfma_f32_16x16x32_f16 v[68:71], v[186:189], v[146:149], 0
	v_mfma_f32_16x16x32_f16 v[72:75], v[178:181], v[154:157], 0
	v_mfma_f32_16x16x32_f16 v[76:79], v[186:189], v[154:157], 0
	v_mfma_f32_16x16x32_f16 v[80:83], v[178:181], v[162:165], 0
	v_mfma_f32_16x16x32_f16 v[84:87], v[186:189], v[162:165], 0
	v_mfma_f32_16x16x32_f16 v[88:91], v[178:181], v[170:173], 0
	v_mfma_f32_16x16x32_f16 v[92:95], v[186:189], v[170:173], 0
	v_mfma_f32_16x16x32_f16 v[64:67], v[182:185], v[150:153], v[64:67]
	v_mfma_f32_16x16x32_f16 v[68:71], v[190:193], v[150:153], v[68:71]
	v_mfma_f32_16x16x32_f16 v[72:75], v[182:185], v[158:161], v[72:75]
	v_mfma_f32_16x16x32_f16 v[76:79], v[190:193], v[158:161], v[76:79]
	v_mfma_f32_16x16x32_f16 v[80:83], v[182:185], v[166:169], v[80:83]
	v_mfma_f32_16x16x32_f16 v[84:87], v[190:193], v[166:169], v[84:87]
	v_mfma_f32_16x16x32_f16 v[88:91], v[182:185], v[174:177], v[88:91]
	v_mfma_f32_16x16x32_f16 v[92:95], v[190:193], v[174:177], v[92:95]
	s_setprio 0
	s_barrier
	ds_read_b128 v[130:133], v224
	ds_read_b128 v[134:137], v224 offset:1024
	ds_read_b128 v[138:141], v224 offset:2048
	ds_read_b128 v[142:145], v224 offset:3072
	ds_read_b128 v[178:181], v229
	ds_read_b128 v[182:185], v229 offset:1024
	ds_read_b128 v[186:189], v229 offset:2048
	ds_read_b128 v[190:193], v229 offset:3072
	ds_read_b128 v[146:149], v225
	ds_read_b128 v[150:153], v225 offset:1024
	ds_read_b128 v[154:157], v226
	ds_read_b128 v[158:161], v226 offset:1024
	ds_read_b128 v[162:165], v227
	ds_read_b128 v[166:169], v227 offset:1024
	ds_read_b128 v[170:173], v228
	ds_read_b128 v[174:177], v228 offset:1024
	v_readlane_b32 s12, v248, s9
	s_mov_b32 m0, s27
	s_nop 1
	v_add_u32_e32 v251, s12, v249
	global_load_lds_dwordx4 v251, s[18:19]
	v_add_u32_e32 v251, s12, v250
	s_mov_b32 m0, s28
	s_nop 0
	global_load_lds_dwordx4 v251, s[18:19]
	s_waitcnt vmcnt(8) lgkmcnt(0)
	s_barrier
	s_setprio 1
	v_mfma_f32_16x16x32_f16 v[124:127], v[130:133], v[146:149], v[124:127]
	v_mfma_f32_16x16x32_f16 v[120:123], v[138:141], v[146:149], v[120:123]
	v_mfma_f32_16x16x32_f16 v[116:119], v[130:133], v[154:157], v[116:119]
	v_mfma_f32_16x16x32_f16 v[112:115], v[138:141], v[154:157], v[112:115]
	v_mfma_f32_16x16x32_f16 v[108:111], v[130:133], v[162:165], v[108:111]
	v_mfma_f32_16x16x32_f16 v[104:107], v[138:141], v[162:165], v[104:107]
	v_mfma_f32_16x16x32_f16 v[100:103], v[130:133], v[170:173], v[100:103]
	v_mfma_f32_16x16x32_f16 v[96:99], v[138:141], v[170:173], v[96:99]
	v_mfma_f32_16x16x32_f16 v[124:127], v[134:137], v[150:153], v[124:127]
	v_mfma_f32_16x16x32_f16 v[120:123], v[142:145], v[150:153], v[120:123]
	v_mfma_f32_16x16x32_f16 v[116:119], v[134:137], v[158:161], v[116:119]
	v_mfma_f32_16x16x32_f16 v[112:115], v[142:145], v[158:161], v[112:115]
	v_mfma_f32_16x16x32_f16 v[108:111], v[134:137], v[166:169], v[108:111]
	v_mfma_f32_16x16x32_f16 v[104:107], v[142:145], v[166:169], v[104:107]
	v_mfma_f32_16x16x32_f16 v[100:103], v[134:137], v[174:177], v[100:103]
	v_mfma_f32_16x16x32_f16 v[96:99], v[142:145], v[174:177], v[96:99]
	v_mfma_f32_16x16x32_f16 v[52:55], v[178:181], v[146:149], v[52:55]
	v_mfma_f32_16x16x32_f16 v[40:43], v[186:189], v[146:149], v[40:43]
	v_mfma_f32_16x16x32_f16 v[36:39], v[178:181], v[154:157], v[36:39]
	v_mfma_f32_16x16x32_f16 v[32:35], v[186:189], v[154:157], v[32:35]
	v_mfma_f32_16x16x32_f16 v[28:31], v[178:181], v[162:165], v[28:31]
	v_mfma_f32_16x16x32_f16 v[24:27], v[186:189], v[162:165], v[24:27]
	v_mfma_f32_16x16x32_f16 v[20:23], v[178:181], v[170:173], v[20:23]
	v_mfma_f32_16x16x32_f16 v[16:19], v[186:189], v[170:173], v[16:19]
	v_mfma_f32_16x16x32_f16 v[52:55], v[182:185], v[150:153], v[52:55]
	v_mfma_f32_16x16x32_f16 v[40:43], v[190:193], v[150:153], v[40:43]
	v_mfma_f32_16x16x32_f16 v[36:39], v[182:185], v[158:161], v[36:39]
	v_mfma_f32_16x16x32_f16 v[32:35], v[190:193], v[158:161], v[32:35]
	v_mfma_f32_16x16x32_f16 v[28:31], v[182:185], v[166:169], v[28:31]
	v_mfma_f32_16x16x32_f16 v[24:27], v[190:193], v[166:169], v[24:27]
	v_mfma_f32_16x16x32_f16 v[20:23], v[182:185], v[174:177], v[20:23]
	v_mfma_f32_16x16x32_f16 v[16:19], v[190:193], v[174:177], v[16:19]
	s_setprio 0
	s_barrier
	ds_read_b128 v[146:149], v230
	ds_read_b128 v[150:153], v230 offset:1024
	ds_read_b128 v[154:157], v231
	ds_read_b128 v[158:161], v231 offset:1024
	ds_read_b128 v[162:165], v232
	ds_read_b128 v[166:169], v232 offset:1024
	ds_read_b128 v[170:173], v233
	ds_read_b128 v[174:177], v233 offset:1024
	s_mov_b32 m0, s37
	v_add_u32_e32 v194, 0x48000, v129
	global_load_lds_dwordx4 v129, s[10:11]
	s_mov_b32 m0, s38
	s_add_i32 s12, s8, 3
	global_load_lds_dwordx4 v194, s[10:11]
	v_readlane_b32 s13, v248, s12
	s_mov_b32 m0, s39
	s_nop 1
	v_add_u32_e32 v194, s13, v206
	global_load_lds_dwordx4 v194, s[18:19]
	v_add_u32_e32 v194, s13, v213
	s_mov_b32 m0, s40
	s_nop 0
	global_load_lds_dwordx4 v194, s[18:19]
	s_mov_b32 m0, s41
	v_add_u32_e32 v194, 0x90000, v129
	global_load_lds_dwordx4 v194, s[10:11]
	v_add_u32_e32 v194, 0xd8000, v129
	s_mov_b32 m0, s42
	s_nop 0
	global_load_lds_dwordx4 v194, s[10:11]
	s_waitcnt vmcnt(8) lgkmcnt(0)
	s_barrier
	s_setprio 1
	v_mfma_f32_16x16x32_f16 v[12:15], v[130:133], v[146:149], v[12:15]
	v_mfma_f32_16x16x32_f16 v[8:11], v[138:141], v[146:149], v[8:11]
	v_mfma_f32_16x16x32_f16 v[4:7], v[130:133], v[154:157], v[4:7]
	v_mfma_f32_16x16x32_f16 v[0:3], v[138:141], v[154:157], v[0:3]
	v_mfma_f32_16x16x32_f16 v[44:47], v[130:133], v[162:165], v[44:47]
	v_mfma_f32_16x16x32_f16 v[48:51], v[138:141], v[162:165], v[48:51]
	v_mfma_f32_16x16x32_f16 v[56:59], v[130:133], v[170:173], v[56:59]
	v_mfma_f32_16x16x32_f16 v[60:63], v[138:141], v[170:173], v[60:63]
	v_mfma_f32_16x16x32_f16 v[12:15], v[134:137], v[150:153], v[12:15]
	v_mfma_f32_16x16x32_f16 v[8:11], v[142:145], v[150:153], v[8:11]
	v_mfma_f32_16x16x32_f16 v[4:7], v[134:137], v[158:161], v[4:7]
	v_mfma_f32_16x16x32_f16 v[0:3], v[142:145], v[158:161], v[0:3]
	v_mfma_f32_16x16x32_f16 v[44:47], v[134:137], v[166:169], v[44:47]
	v_mfma_f32_16x16x32_f16 v[48:51], v[142:145], v[166:169], v[48:51]
	v_mfma_f32_16x16x32_f16 v[56:59], v[134:137], v[174:177], v[56:59]
	v_mfma_f32_16x16x32_f16 v[60:63], v[142:145], v[174:177], v[60:63]
	v_mfma_f32_16x16x32_f16 v[64:67], v[178:181], v[146:149], v[64:67]
	v_mfma_f32_16x16x32_f16 v[68:71], v[186:189], v[146:149], v[68:71]
	v_mfma_f32_16x16x32_f16 v[72:75], v[178:181], v[154:157], v[72:75]
	v_mfma_f32_16x16x32_f16 v[76:79], v[186:189], v[154:157], v[76:79]
	v_mfma_f32_16x16x32_f16 v[80:83], v[178:181], v[162:165], v[80:83]
	v_mfma_f32_16x16x32_f16 v[84:87], v[186:189], v[162:165], v[84:87]
	v_mfma_f32_16x16x32_f16 v[88:91], v[178:181], v[170:173], v[88:91]
	v_mfma_f32_16x16x32_f16 v[92:95], v[186:189], v[170:173], v[92:95]
	v_mfma_f32_16x16x32_f16 v[64:67], v[182:185], v[150:153], v[64:67]
	v_mfma_f32_16x16x32_f16 v[68:71], v[190:193], v[150:153], v[68:71]
	v_mfma_f32_16x16x32_f16 v[72:75], v[182:185], v[158:161], v[72:75]
	v_mfma_f32_16x16x32_f16 v[76:79], v[190:193], v[158:161], v[76:79]
	v_mfma_f32_16x16x32_f16 v[80:83], v[182:185], v[166:169], v[80:83]
	v_mfma_f32_16x16x32_f16 v[84:87], v[190:193], v[166:169], v[84:87]
	v_mfma_f32_16x16x32_f16 v[88:91], v[182:185], v[174:177], v[88:91]
	v_mfma_f32_16x16x32_f16 v[92:95], v[190:193], v[174:177], v[92:95]
	s_setprio 0
	s_addk_i32 s7, 0x100
	s_cmp_lt_u32 s8, 32
	s_mov_b32 s8, s9
	s_barrier
